# B4 (layer 0): compute-workgroup count derived for at least four GEMM rounds, so about 64 workgroups serve the weight-conversion queue while the expert GEMM runs
# baseline (speedup 1.0000x reference)
.LBB0_1419:
	v_writelane_b32 v253, s62, 40
	s_nop 1
	v_writelane_b32 v253, s63, 41
	v_writelane_b32 v253, s61, 62
	s_or_b64 exec, exec, s[0:1]
	v_readlane_b32 s8, v253, 31
	v_readlane_b32 s9, v253, 32
	s_waitcnt lgkmcnt(0)
	s_barrier
	v_readlane_b32 s10, v253, 12
	v_readlane_b32 s11, v253, 13
	s_nop 0
	global_load_dword v0, v173, s[8:9] sc1
	global_load_dword v1, v173, s[8:9] offset:256 sc1
	global_load_dword v2, v173, s[8:9] offset:512 sc1
	global_load_dword v3, v173, s[8:9] offset:768 sc1
	global_load_dword v4, v173, s[8:9] offset:1024 sc1
	global_load_dword v5, v173, s[8:9] offset:1280 sc1
	global_load_dword v6, v173, s[8:9] offset:1536 sc1
	global_load_dword v7, v173, s[8:9] offset:1792 sc1
	v_readlane_b32 s30, v253, 9
	s_waitcnt vmcnt(0)
	v_readfirstlane_b32 s0, v0
	s_nop 0
	s_min_i32 s0, s0, 0x2000
	s_addk_i32 s0, 0xff
	s_ashr_i32 s2, s0, 8
	s_nop 0
	v_readfirstlane_b32 s0, v1
	s_nop 0
	s_min_i32 s0, s0, 0x2000
	s_addk_i32 s0, 0xff
	s_ashr_i32 s3, s0, 8
	s_add_i32 s7, s3, s2
	s_nop 0
	v_readfirstlane_b32 s0, v2
	s_nop 0
	s_min_i32 s0, s0, 0x2000
	s_addk_i32 s0, 0xff
	s_ashr_i32 s73, s0, 8
	s_add_i32 s61, s73, s7
	s_nop 0
	v_readfirstlane_b32 s0, v3
	s_nop 0
	s_min_i32 s0, s0, 0x2000
	s_addk_i32 s0, 0xff
	s_ashr_i32 s74, s0, 8
	s_add_i32 s62, s74, s61
	s_nop 0
	v_readfirstlane_b32 s0, v4
	s_nop 0
	s_min_i32 s0, s0, 0x2000
	s_addk_i32 s0, 0xff
	s_ashr_i32 s75, s0, 8
	s_add_i32 s63, s75, s62
	s_nop 0
	v_readfirstlane_b32 s0, v5
	s_nop 0
	s_min_i32 s0, s0, 0x2000
	s_addk_i32 s0, 0xff
	s_ashr_i32 s84, s0, 8
	s_add_i32 s64, s84, s63
	s_nop 0
	v_readfirstlane_b32 s0, v6
	s_nop 0
	s_min_i32 s0, s0, 0x2000
	s_addk_i32 s0, 0xff
	s_ashr_i32 s65, s0, 8
	s_add_i32 s43, s65, s64
	s_nop 0
	v_readfirstlane_b32 s0, v7
	s_min_i32 s0, s0, 0x2000
	s_addk_i32 s0, 0xff
	s_ashr_i32 s66, s0, 8
	s_add_i32 s0, s66, s43
	s_cmp_lt_i32 s0, 1
	s_mul_i32 s8, s0, 11
	s_cselect_b64 s[0:1], -1, 0
	s_or_b64 s[0:1], s[10:11], s[0:1]
	s_and_b64 vcc, exec, s[0:1]
	s_cbranch_vccnz .LBB0_1421
	s_add_i32 s0, s8, -1
	v_readlane_b32 s13, v253, 9
	s_add_i32 s1, s0, s13
	s_ashr_i32 s9, s1, 31
	v_readlane_b32 s10, v253, 29
	s_xor_b32 s9, s9, s10
	s_abs_i32 s1, s1
	v_readlane_b32 s10, v253, 49
	s_mul_hi_u32 s10, s1, s10
	v_readlane_b32 s14, v253, 50
	s_mul_i32 s11, s10, s14
	s_sub_i32 s1, s1, s11
	s_add_i32 s11, s10, 1
	s_sub_i32 s12, s1, s14
	s_cmp_ge_u32 s1, s14
	s_cselect_b32 s10, s11, s10
	s_cselect_b32 s1, s12, s1
	s_add_i32 s11, s10, 1
	s_cmp_ge_u32 s1, s14
	s_cselect_b32 s1, s11, s10
	s_xor_b32 s1, s1, s9
	s_sub_i32 s1, s1, s9
	s_max_i32 s1, s1, 4
	s_abs_i32 s9, s1
	v_cvt_f32_u32_e32 v0, s9
	s_sub_i32 s10, 0, s9
	s_add_i32 s0, s1, s0
	s_xor_b32 s1, s0, s1
	v_rcp_iflag_f32_e32 v0, v0
	s_abs_i32 s0, s0
	s_ashr_i32 s1, s1, 31
	v_mul_f32_e32 v0, 0x4f7ffffe, v0
	v_cvt_u32_f32_e32 v0, v0
	s_nop 0
	v_readfirstlane_b32 s11, v0
	s_mul_i32 s10, s10, s11
	s_mul_hi_u32 s10, s11, s10
	s_add_i32 s11, s11, s10
	s_mul_hi_u32 s10, s0, s11
	s_mul_i32 s11, s10, s9
	s_sub_i32 s0, s0, s11
	s_add_i32 s11, s10, 1
	s_sub_i32 s12, s0, s9
	s_cmp_ge_u32 s0, s9
	s_cselect_b32 s10, s11, s10
	s_cselect_b32 s0, s12, s0
	s_add_i32 s11, s10, 1
	s_cmp_ge_u32 s0, s9
	s_cselect_b32 s0, s11, s10
	s_xor_b32 s0, s0, s1
	s_sub_i32 s0, s0, s1
	s_add_i32 s0, s0, 7
	s_and_b32 s0, s0, -8
	s_min_i32 s30, s0, s13
